# MoE epilogues: P10 bias loads all in flight before first wait; P11 second bias pair hoisted next to the first (no store-drain wait)
# speedup vs baseline: 1.0053x; 1.0053x over previous
; __device__ __forceinline__ unsigned pk4f8(float a, float b, float c, float d) { int r = 0; r = __builtin_amdgcn_cvt_pk_fp8_f32(a, b, r, false); r = __builtin_amdgcn_cvt_pk_fp8_f32(c, d, r, true); return (unsigned)r; }
; __device__ __forceinline__ float sigm(float x) { return __builtin_amdgcn_rcpf(1.f + __expf(-x)); }
;     __device__ __forceinline__ void operator()(const f32x4 (&acc)[2][2][4][2], const Unit& u, int wr, int wc, int fr, int fq) const {
;         const int row0 = u.pm * BM + wr * 64 + fr, colg = u.pn * 128 + wc * 32 + 8 * fq; const int e = tile_e[u.pm];
;         const float* bp = bgu + (size_t)e * 4096 + colg;
;         const f32x4 bg0 = *(const f32x4*)(bp), bg1 = *(const f32x4*)(bp + 4), bu0 = *(const f32x4*)(bp + 2048), bu1 = *(const f32x4*)(bp + 2052);
; #pragma unroll
;         for (int ai = 0; ai < 2; ++ai)
; #pragma unroll
;             for (int m = 0; m < 4; ++m) { const size_t r = (size_t)(row0 + ai * HALF + m * 16);
;                 constexpr float DS = 1.f / (F8_SX * F8_SW);
;                 const f32x4 ga = acc[ai][0][m][0] * DS + bg0, gb = acc[ai][0][m][1] * DS + bg1, ua = acc[ai][1][m][0] * DS + bu0, ub = acc[ai][1][m][1] * DS + bu1;
;                 float o[8];
; #pragma unroll
;                 for (int j = 0; j < 4; ++j) { const float g = fminf(ga[j], 7.f), up = fminf(fmaxf(ua[j], -7.f), 7.f); o[j] = F8_SA * (up + 1.f) * g * sigm(1.702f * g);
;                                               const float g2 = fminf(gb[j], 7.f), up2 = fminf(fmaxf(ub[j], -7.f), 7.f); o[4 + j] = F8_SA * (up2 + 1.f) * g2 * sigm(1.702f * g2); }
;                 v2u w; w.x = pk4f8(o[0], o[1], o[2], o[3]); w.y = pk4f8(o[4], o[5], o[6], o[7]);
;                 *(v2u*)(ACT + r * FF + colg) = w; }
.LBB0_1922:
	s_lshl_b32 s2, s43, 2
	s_add_i32 s2, s2, 0
	s_add_i32 s2, s2, 0x20100
	s_nop 15
	s_nop 15
	v_mov_b32_e32 v2, s2
	ds_read_b32 v2, v2
	v_lshl_or_b32 v20, s0, 7, v196
	v_ashrrev_i32_e32 v21, 31, v20
	v_lshl_add_u32 v22, s43, 8, v194
	s_waitcnt lgkmcnt(0)
	v_ashrrev_i32_e32 v3, 31, v2
	v_lshlrev_b64 v[2:3], 14, v[2:3]
	v_lshl_add_u64 v[2:3], s[80:81], 0, v[2:3]
	v_lshl_add_u64 v[2:3], v[20:21], 2, v[2:3]
	global_load_dwordx4 v[14:17], v[2:3], off
	global_load_dwordx4 v[6:9], v[2:3], off offset:16
	v_add_co_u32_e32 v4, vcc, s52, v2
	s_nop 1
	v_addc_co_u32_e32 v5, vcc, 0, v3, vcc
	v_lshl_add_u64 v[2:3], v[2:3], 0, s[38:39]
	global_load_dwordx4 v[10:13], v[4:5], off
	global_load_dwordx4 v[2:5], v[2:3], off offset:16
	s_waitcnt vmcnt(2)
	v_fmamk_f32 v18, v158, 0x3a000000, v14
	v_fmamk_f32 v24, v155, 0x3a000000, v7
	v_min_f32_e32 v18, 0x40e00000, v18
	v_min_f32_e32 v24, 0x40e00000, v24
	v_fmamk_f32 v19, v154, 0x3a000000, v6
	v_fmamk_f32 v25, v160, 0x3a000000, v16
	v_mul_f32_e32 v175, 0x3fd9db23, v18
	v_mul_f32_e32 v183, 0x3fd9db23, v24
	v_min_f32_e32 v19, 0x40e00000, v19
	v_min_f32_e32 v25, 0x40e00000, v25
	v_mul_f32_e32 v175, 0xbfb8aa3b, v175
	v_mul_f32_e32 v183, 0xbfb8aa3b, v183
	v_mul_f32_e32 v177, 0x3fd9db23, v19
	v_mul_f32_e32 v184, 0x3fd9db23, v25
	v_exp_f32_e32 v175, v175
	v_exp_f32_e32 v183, v183
	v_fmamk_f32 v27, v161, 0x3a000000, v17
	v_mul_f32_e32 v177, 0xbfb8aa3b, v177
	v_mul_f32_e32 v184, 0xbfb8aa3b, v184
	v_min_f32_e32 v27, 0x40e00000, v27
	v_exp_f32_e32 v177, v177
	v_exp_f32_e32 v184, v184
	v_fmamk_f32 v23, v159, 0x3a000000, v15
	v_mul_f32_e32 v186, 0x3fd9db23, v27
	v_min_f32_e32 v23, 0x40e00000, v23
	v_mul_f32_e32 v186, 0xbfb8aa3b, v186
	v_mul_f32_e32 v182, 0x3fd9db23, v23
	v_exp_f32_e32 v186, v186
	v_mul_f32_e32 v182, 0xbfb8aa3b, v182
	v_exp_f32_e32 v182, v182
	v_fmamk_f32 v26, v156, 0x3a000000, v8
	v_min_f32_e32 v26, 0x40e00000, v26
	v_mul_f32_e32 v185, 0x3fd9db23, v26
	v_mul_f32_e32 v185, 0xbfb8aa3b, v185
	v_exp_f32_e32 v185, v185
	s_waitcnt vmcnt(1)
	v_fmamk_f32 v28, v126, 0x3a000000, v10
	v_med3_f32 v28, v28, s55, v199
	s_waitcnt vmcnt(0)
	v_fmamk_f32 v31, v123, 0x3a000000, v3
	v_med3_f32 v31, v31, s55, v199
	v_fmamk_f32 v29, v122, 0x3a000000, v2
	v_fmamk_f32 v32, v128, 0x3a000000, v12
	v_add_f32_e32 v28, 1.0, v28
	v_add_f32_e32 v31, 1.0, v31
	v_med3_f32 v29, v29, s55, v199
	v_med3_f32 v32, v32, s55, v199
	v_mul_f32_e32 v28, 4.0, v28
	v_mul_f32_e32 v31, 4.0, v31
	v_add_f32_e32 v29, 1.0, v29
	v_add_f32_e32 v32, 1.0, v32
	v_mul_f32_e32 v18, v18, v28
	v_mul_f32_e32 v24, v24, v31
	v_add_f32_e32 v28, 1.0, v175
	v_add_f32_e32 v31, 1.0, v183
	v_mul_f32_e32 v29, 4.0, v29
	v_mul_f32_e32 v32, 4.0, v32
	v_rcp_f32_e32 v28, v28
	v_rcp_f32_e32 v31, v31
	v_mul_f32_e32 v19, v19, v29
	v_mul_f32_e32 v25, v25, v32
	v_add_f32_e32 v29, 1.0, v177
	v_add_f32_e32 v32, 1.0, v184
	v_fmamk_f32 v30, v127, 0x3a000000, v11
	v_rcp_f32_e32 v29, v29
	v_rcp_f32_e32 v32, v32
	v_med3_f32 v30, v30, s55, v199
	v_fmamk_f32 v173, v129, 0x3a000000, v13
	v_add_f32_e32 v30, 1.0, v30
	v_mul_f32_e32 v18, v28, v18
	v_mul_f32_e32 v28, v31, v24
	v_add_f32_e32 v24, 1.0, v186
	v_med3_f32 v173, v173, s55, v199
	v_mul_f32_e32 v30, 4.0, v30
	v_rcp_f32_e32 v24, v24
	v_mul_f32_e32 v23, v23, v30
	v_add_f32_e32 v30, 1.0, v182
	v_mul_f32_e32 v19, v29, v19
	v_mul_f32_e32 v29, v32, v25
	v_add_f32_e32 v25, 1.0, v173
	v_rcp_f32_e32 v30, v30
	v_mul_f32_e32 v25, 4.0, v25
	v_mul_f32_e32 v25, v27, v25
	v_mul_f32_e32 v27, v24, v25
	v_fmamk_f32 v24, v157, 0x3a000000, v9
	v_min_f32_e32 v24, 0x40e00000, v24
	v_mul_f32_e32 v23, v30, v23
	v_mul_f32_e32 v30, 0x3fd9db23, v24
	v_mul_f32_e32 v30, 0xbfb8aa3b, v30
	v_fmamk_f32 v33, v124, 0x3a000000, v4
	v_fmamk_f32 v25, v125, 0x3a000000, v5
	v_exp_f32_e32 v30, v30
	v_med3_f32 v33, v33, s55, v199
	v_med3_f32 v25, v25, s55, v199
	v_add_f32_e32 v33, 1.0, v33
	v_add_f32_e32 v25, 1.0, v25
	v_mul_f32_e32 v33, 4.0, v33
	v_mul_f32_e32 v25, 4.0, v25
	v_mul_f32_e32 v26, v26, v33
	v_add_f32_e32 v33, 1.0, v185
	v_mul_f32_e32 v31, v24, v25
	v_add_f32_e32 v24, 1.0, v30
	v_rcp_f32_e32 v33, v33
	v_rcp_f32_e32 v30, v24
	v_mov_b32_e32 v24, v171
	v_mov_b32_e32 v25, v171
	v_cvt_pk_fp8_f32 v24, v18, v23
	v_cvt_pk_fp8_f32 v25, v19, v28
	v_mul_f32_e32 v26, v33, v26
	v_mul_f32_e32 v18, v30, v31
	v_ashrrev_i32_e32 v23, 31, v22
	v_cvt_pk_fp8_f32 v24, v29, v27 op_sel:[0,0,1]
	v_cvt_pk_fp8_f32 v25, v26, v18 op_sel:[0,0,1]
	v_lshlrev_b64 v[18:19], 11, v[22:23]
	v_lshl_add_u64 v[18:19], s[22:23], 0, v[18:19]
	v_fmamk_f32 v23, v150, 0x3a000000, v14
	v_lshl_add_u64 v[18:19], v[18:19], 0, v[20:21]
	v_min_f32_e32 v23, 0x40e00000, v23
	global_store_dwordx2 v[18:19], v[24:25], off
	v_mul_f32_e32 v24, 0x3fd9db23, v23
	v_mul_f32_e32 v24, 0xbfb8aa3b, v24
	v_exp_f32_e32 v25, v24
	v_fmamk_f32 v26, v118, 0x3a000000, v10
	v_med3_f32 v26, v26, s55, v199
	v_add_f32_e32 v26, 1.0, v26
	v_add_f32_e32 v25, 1.0, v25
	v_rcp_f32_e32 v25, v25
	v_mul_f32_e32 v26, 4.0, v26
	v_mul_f32_e32 v23, v23, v26
	v_fmamk_f32 v26, v114, 0x3a000000, v2
	v_mul_f32_e32 v23, v25, v23
	v_fmamk_f32 v25, v146, 0x3a000000, v6
	v_min_f32_e32 v25, 0x40e00000, v25
	v_mul_f32_e32 v27, 0x3fd9db23, v25
	v_mul_f32_e32 v27, 0xbfb8aa3b, v27
	v_exp_f32_e32 v27, v27
	v_med3_f32 v26, v26, s55, v199
	v_add_f32_e32 v26, 1.0, v26
	v_mul_f32_e32 v26, 4.0, v26
	v_mul_f32_e32 v25, v25, v26
	v_add_f32_e32 v26, 1.0, v27
	v_fmamk_f32 v27, v151, 0x3a000000, v15
	v_min_f32_e32 v27, 0x40e00000, v27
	v_mul_f32_e32 v28, 0x3fd9db23, v27
	v_mul_f32_e32 v28, 0xbfb8aa3b, v28
	v_rcp_f32_e32 v26, v26
	v_exp_f32_e32 v28, v28
	v_or_b32_e32 v24, 16, v22
	v_mul_f32_e32 v25, v26, v25
	v_fmamk_f32 v26, v119, 0x3a000000, v11
	v_add_f32_e32 v28, 1.0, v28
; __device__ __forceinline__ unsigned pk4f8(float a, float b, float c, float d) { int r = 0; r = __builtin_amdgcn_cvt_pk_fp8_f32(a, b, r, false); r = __builtin_amdgcn_cvt_pk_fp8_f32(c, d, r, true); return (unsigned)r; }
; __device__ __forceinline__ float sigm(float x) { return __builtin_amdgcn_rcpf(1.f + __expf(-x)); }
;     __device__ __forceinline__ void operator()(const f32x4 (&acc)[2][2][4][2], const Unit& u, int wr, int wc, int fr, int fq) const {
;     ...
;             for (int m = 0; m < 4; ++m) { const size_t r = (size_t)(row0 + ai * HALF + m * 16);
;                 constexpr float DS = 1.f / (F8_SX * F8_SW);
;                 const f32x4 ga = acc[ai][0][m][0] * DS + bg0, gb = acc[ai][0][m][1] * DS + bg1, ua = acc[ai][1][m][0] * DS + bu0, ub = acc[ai][1][m][1] * DS + bu1;
;                 float o[8];
; #pragma unroll
;                 for (int j = 0; j < 4; ++j) { const float g = fminf(ga[j], 7.f), up = fminf(fmaxf(ua[j], -7.f), 7.f); o[j] = F8_SA * (up + 1.f) * g * sigm(1.702f * g);
;                                               const float g2 = fminf(gb[j], 7.f), up2 = fminf(fmaxf(ub[j], -7.f), 7.f); o[4 + j] = F8_SA * (up2 + 1.f) * g2 * sigm(1.702f * g2); }
;                 v2u w; w.x = pk4f8(o[0], o[1], o[2], o[3]); w.y = pk4f8(o[4], o[5], o[6], o[7]);
;                 *(v2u*)(ACT + r * FF + colg) = w; }
	v_med3_f32 v26, v26, s55, v199
	v_rcp_f32_e32 v28, v28
	v_add_f32_e32 v26, 1.0, v26
	v_mul_f32_e32 v26, 4.0, v26
	v_mul_f32_e32 v26, v27, v26
	v_mul_f32_e32 v27, v28, v26
	v_fmamk_f32 v26, v147, 0x3a000000, v7
	v_min_f32_e32 v26, 0x40e00000, v26
	v_mul_f32_e32 v29, 0x3fd9db23, v26
	v_mul_f32_e32 v29, 0xbfb8aa3b, v29
	v_fmamk_f32 v28, v115, 0x3a000000, v3
	v_exp_f32_e32 v29, v29
	v_med3_f32 v28, v28, s55, v199
	v_add_f32_e32 v28, 1.0, v28
	v_mul_f32_e32 v28, 4.0, v28
	v_mul_f32_e32 v26, v26, v28
	v_add_f32_e32 v28, 1.0, v29
	v_fmamk_f32 v29, v152, 0x3a000000, v16
	v_min_f32_e32 v29, 0x40e00000, v29
	v_mul_f32_e32 v30, 0x3fd9db23, v29
	v_mul_f32_e32 v30, 0xbfb8aa3b, v30
	v_rcp_f32_e32 v28, v28
	v_exp_f32_e32 v30, v30
	v_mul_f32_e32 v28, v28, v26
	v_fmamk_f32 v26, v120, 0x3a000000, v12
	v_add_f32_e32 v30, 1.0, v30
	v_med3_f32 v26, v26, s55, v199
	v_rcp_f32_e32 v30, v30
	v_add_f32_e32 v26, 1.0, v26
	v_mul_f32_e32 v26, 4.0, v26
	v_mul_f32_e32 v26, v29, v26
	v_mul_f32_e32 v29, v30, v26
	v_fmamk_f32 v26, v148, 0x3a000000, v8
	v_min_f32_e32 v26, 0x40e00000, v26
	v_mul_f32_e32 v31, 0x3fd9db23, v26
	v_mul_f32_e32 v31, 0xbfb8aa3b, v31
	v_fmamk_f32 v30, v116, 0x3a000000, v4
	v_exp_f32_e32 v31, v31
	v_med3_f32 v30, v30, s55, v199
	v_add_f32_e32 v30, 1.0, v30
	v_mul_f32_e32 v30, 4.0, v30
	v_mul_f32_e32 v26, v26, v30
	v_add_f32_e32 v30, 1.0, v31
	v_fmamk_f32 v31, v153, 0x3a000000, v17
	v_min_f32_e32 v31, 0x40e00000, v31
	v_mul_f32_e32 v32, 0x3fd9db23, v31
	v_mul_f32_e32 v32, 0xbfb8aa3b, v32
	v_rcp_f32_e32 v30, v30
	v_exp_f32_e32 v32, v32
	v_mul_f32_e32 v30, v30, v26
	v_fmamk_f32 v26, v121, 0x3a000000, v13
	v_add_f32_e32 v32, 1.0, v32
	v_med3_f32 v26, v26, s55, v199
	v_rcp_f32_e32 v32, v32
	v_add_f32_e32 v26, 1.0, v26
	v_mul_f32_e32 v26, 4.0, v26
	v_mul_f32_e32 v26, v31, v26
	v_mul_f32_e32 v31, v32, v26
	v_fmamk_f32 v26, v149, 0x3a000000, v9
	v_min_f32_e32 v26, 0x40e00000, v26
	v_mul_f32_e32 v33, 0x3fd9db23, v26
	v_mul_f32_e32 v33, 0xbfb8aa3b, v33
	v_fmamk_f32 v32, v117, 0x3a000000, v5
	v_exp_f32_e32 v33, v33
	v_med3_f32 v32, v32, s55, v199
	v_add_f32_e32 v32, 1.0, v32
	v_mul_f32_e32 v32, 4.0, v32
	v_mul_f32_e32 v32, v26, v32
	v_add_f32_e32 v26, 1.0, v33
	v_rcp_f32_e32 v33, v26
	v_mov_b32_e32 v26, v171
	v_cvt_pk_fp8_f32 v26, v23, v27
	v_mov_b32_e32 v27, v171
	v_cvt_pk_fp8_f32 v27, v25, v28
	v_mul_f32_e32 v23, v33, v32
	v_ashrrev_i32_e32 v25, 31, v24
	v_cvt_pk_fp8_f32 v26, v29, v31 op_sel:[0,0,1]
	v_cvt_pk_fp8_f32 v27, v30, v23 op_sel:[0,0,1]
	v_lshlrev_b64 v[24:25], 11, v[24:25]
	v_lshl_add_u64 v[24:25], s[22:23], 0, v[24:25]
	v_fmamk_f32 v23, v142, 0x3a000000, v14
	v_lshl_add_u64 v[24:25], v[24:25], 0, v[20:21]
	v_min_f32_e32 v23, 0x40e00000, v23
	global_store_dwordx2 v[24:25], v[26:27], off
	v_mul_f32_e32 v24, 0x3fd9db23, v23
	v_mul_f32_e32 v24, 0xbfb8aa3b, v24
	v_exp_f32_e32 v25, v24
	v_fmamk_f32 v26, v110, 0x3a000000, v10
	v_med3_f32 v26, v26, s55, v199
	v_add_f32_e32 v26, 1.0, v26
	v_add_f32_e32 v25, 1.0, v25
	v_rcp_f32_e32 v25, v25
	v_mul_f32_e32 v26, 4.0, v26
	v_mul_f32_e32 v23, v23, v26
	v_fmamk_f32 v26, v106, 0x3a000000, v2
	v_mul_f32_e32 v23, v25, v23
	v_fmamk_f32 v25, v138, 0x3a000000, v6
	v_min_f32_e32 v25, 0x40e00000, v25
	v_mul_f32_e32 v27, 0x3fd9db23, v25
	v_mul_f32_e32 v27, 0xbfb8aa3b, v27
	v_exp_f32_e32 v27, v27
	v_med3_f32 v26, v26, s55, v199
	v_add_f32_e32 v26, 1.0, v26
	v_mul_f32_e32 v26, 4.0, v26
	v_mul_f32_e32 v25, v25, v26
	v_add_f32_e32 v26, 1.0, v27
	v_fmamk_f32 v27, v143, 0x3a000000, v15
	v_min_f32_e32 v27, 0x40e00000, v27
	v_mul_f32_e32 v28, 0x3fd9db23, v27
	v_mul_f32_e32 v28, 0xbfb8aa3b, v28
	v_rcp_f32_e32 v26, v26
	v_exp_f32_e32 v28, v28
	v_or_b32_e32 v24, 32, v22
	v_or_b32_e32 v22, 48, v22
	v_mul_f32_e32 v25, v26, v25
	v_fmamk_f32 v26, v111, 0x3a000000, v11
	v_add_f32_e32 v28, 1.0, v28
	v_med3_f32 v26, v26, s55, v199
	v_rcp_f32_e32 v28, v28
	v_add_f32_e32 v26, 1.0, v26
	v_mul_f32_e32 v26, 4.0, v26
	v_mul_f32_e32 v26, v27, v26
	v_mul_f32_e32 v27, v28, v26
	v_fmamk_f32 v26, v139, 0x3a000000, v7
	v_min_f32_e32 v26, 0x40e00000, v26
	v_mul_f32_e32 v29, 0x3fd9db23, v26
	v_mul_f32_e32 v29, 0xbfb8aa3b, v29
	v_fmamk_f32 v28, v107, 0x3a000000, v3
	v_exp_f32_e32 v29, v29
	v_med3_f32 v28, v28, s55, v199
	v_add_f32_e32 v28, 1.0, v28
	v_mul_f32_e32 v28, 4.0, v28
	v_mul_f32_e32 v26, v26, v28
	v_add_f32_e32 v28, 1.0, v29
	v_fmamk_f32 v29, v144, 0x3a000000, v16
	v_min_f32_e32 v29, 0x40e00000, v29
	v_mul_f32_e32 v30, 0x3fd9db23, v29
	v_mul_f32_e32 v30, 0xbfb8aa3b, v30
	v_rcp_f32_e32 v28, v28
	v_exp_f32_e32 v30, v30
	v_mul_f32_e32 v28, v28, v26
	v_fmamk_f32 v26, v112, 0x3a000000, v12
	v_add_f32_e32 v30, 1.0, v30
	v_med3_f32 v26, v26, s55, v199
	v_rcp_f32_e32 v30, v30
	v_add_f32_e32 v26, 1.0, v26
	v_mul_f32_e32 v26, 4.0, v26
	v_mul_f32_e32 v26, v29, v26
	v_mul_f32_e32 v29, v30, v26
	v_fmamk_f32 v26, v140, 0x3a000000, v8
	v_min_f32_e32 v26, 0x40e00000, v26
	v_mul_f32_e32 v31, 0x3fd9db23, v26
	v_mul_f32_e32 v31, 0xbfb8aa3b, v31
	v_fmamk_f32 v30, v108, 0x3a000000, v4
	v_exp_f32_e32 v31, v31
	v_med3_f32 v30, v30, s55, v199
	v_add_f32_e32 v30, 1.0, v30
	v_mul_f32_e32 v30, 4.0, v30
	v_mul_f32_e32 v26, v26, v30
	v_add_f32_e32 v30, 1.0, v31
	v_fmamk_f32 v31, v145, 0x3a000000, v17
	v_min_f32_e32 v31, 0x40e00000, v31
	v_mul_f32_e32 v32, 0x3fd9db23, v31
	v_mul_f32_e32 v32, 0xbfb8aa3b, v32
	v_rcp_f32_e32 v30, v30
	v_exp_f32_e32 v32, v32
	v_mul_f32_e32 v30, v30, v26
	v_fmamk_f32 v26, v113, 0x3a000000, v13
	v_add_f32_e32 v32, 1.0, v32
	v_med3_f32 v26, v26, s55, v199
	v_rcp_f32_e32 v32, v32
	v_add_f32_e32 v26, 1.0, v26
	v_mul_f32_e32 v26, 4.0, v26
	v_mul_f32_e32 v26, v31, v26
	v_mul_f32_e32 v31, v32, v26
	v_fmamk_f32 v26, v141, 0x3a000000, v9
; __device__ __forceinline__ unsigned pk4f8(float a, float b, float c, float d) { int r = 0; r = __builtin_amdgcn_cvt_pk_fp8_f32(a, b, r, false); r = __builtin_amdgcn_cvt_pk_fp8_f32(c, d, r, true); return (unsigned)r; }
; __device__ __forceinline__ float sigm(float x) { return __builtin_amdgcn_rcpf(1.f + __expf(-x)); }
;     __device__ __forceinline__ void operator()(const f32x4 (&acc)[2][2][4][2], const Unit& u, int wr, int wc, int fr, int fq) const {
;     ...
; #pragma unroll
;         for (int ai = 0; ai < 2; ++ai)
; #pragma unroll
;             for (int m = 0; m < 4; ++m) { const size_t r = (size_t)(row0 + ai * HALF + m * 16);
;                 constexpr float DS = 1.f / (F8_SX * F8_SW);
;                 const f32x4 ga = acc[ai][0][m][0] * DS + bg0, gb = acc[ai][0][m][1] * DS + bg1, ua = acc[ai][1][m][0] * DS + bu0, ub = acc[ai][1][m][1] * DS + bu1;
;                 float o[8];
; #pragma unroll
;                 for (int j = 0; j < 4; ++j) { const float g = fminf(ga[j], 7.f), up = fminf(fmaxf(ua[j], -7.f), 7.f); o[j] = F8_SA * (up + 1.f) * g * sigm(1.702f * g);
;                                               const float g2 = fminf(gb[j], 7.f), up2 = fminf(fmaxf(ub[j], -7.f), 7.f); o[4 + j] = F8_SA * (up2 + 1.f) * g2 * sigm(1.702f * g2); }
;                 v2u w; w.x = pk4f8(o[0], o[1], o[2], o[3]); w.y = pk4f8(o[4], o[5], o[6], o[7]);
;                 *(v2u*)(ACT + r * FF + colg) = w; }
	v_min_f32_e32 v26, 0x40e00000, v26
	v_mul_f32_e32 v33, 0x3fd9db23, v26
	v_mul_f32_e32 v33, 0xbfb8aa3b, v33
	v_fmamk_f32 v32, v109, 0x3a000000, v5
	v_exp_f32_e32 v33, v33
	v_med3_f32 v32, v32, s55, v199
	v_add_f32_e32 v32, 1.0, v32
	v_mul_f32_e32 v32, 4.0, v32
	v_mul_f32_e32 v32, v26, v32
	v_add_f32_e32 v26, 1.0, v33
	v_rcp_f32_e32 v33, v26
	v_mov_b32_e32 v26, v171
	v_cvt_pk_fp8_f32 v26, v23, v27
	v_mov_b32_e32 v27, v171
	v_cvt_pk_fp8_f32 v27, v25, v28
	v_mul_f32_e32 v23, v33, v32
	v_ashrrev_i32_e32 v25, 31, v24
	v_cvt_pk_fp8_f32 v26, v29, v31 op_sel:[0,0,1]
	v_cvt_pk_fp8_f32 v27, v30, v23 op_sel:[0,0,1]
	v_lshlrev_b64 v[24:25], 11, v[24:25]
	v_lshl_add_u64 v[24:25], s[22:23], 0, v[24:25]
	v_fmamk_f32 v23, v134, 0x3a000000, v14
	v_lshl_add_u64 v[24:25], v[24:25], 0, v[20:21]
	v_min_f32_e32 v23, 0x40e00000, v23
	global_store_dwordx2 v[24:25], v[26:27], off
	v_mul_f32_e32 v24, 0x3fd9db23, v23
	v_mul_f32_e32 v24, 0xbfb8aa3b, v24
	v_exp_f32_e32 v24, v24
	v_fmamk_f32 v25, v102, 0x3a000000, v10
	v_med3_f32 v25, v25, s55, v199
	v_add_f32_e32 v25, 1.0, v25
	v_add_f32_e32 v24, 1.0, v24
	v_rcp_f32_e32 v24, v24
	v_mul_f32_e32 v25, 4.0, v25
	v_mul_f32_e32 v23, v23, v25
	v_fmamk_f32 v25, v98, 0x3a000000, v2
	v_mul_f32_e32 v23, v24, v23
	v_fmamk_f32 v24, v130, 0x3a000000, v6
	v_min_f32_e32 v24, 0x40e00000, v24
	v_mul_f32_e32 v26, 0x3fd9db23, v24
	v_mul_f32_e32 v26, 0xbfb8aa3b, v26
	v_exp_f32_e32 v26, v26
	v_med3_f32 v25, v25, s55, v199
	v_add_f32_e32 v25, 1.0, v25
	v_mul_f32_e32 v25, 4.0, v25
	v_mul_f32_e32 v24, v24, v25
	v_add_f32_e32 v25, 1.0, v26
	v_fmamk_f32 v26, v135, 0x3a000000, v15
	v_min_f32_e32 v26, 0x40e00000, v26
	v_mul_f32_e32 v27, 0x3fd9db23, v26
	v_mul_f32_e32 v27, 0xbfb8aa3b, v27
	v_rcp_f32_e32 v25, v25
	v_exp_f32_e32 v27, v27
	v_mul_f32_e32 v28, v25, v24
	v_fmamk_f32 v24, v103, 0x3a000000, v11
	v_add_f32_e32 v25, 1.0, v27
	v_med3_f32 v24, v24, s55, v199
	v_rcp_f32_e32 v25, v25
	v_add_f32_e32 v24, 1.0, v24
	v_mul_f32_e32 v24, 4.0, v24
	v_mul_f32_e32 v24, v26, v24
	v_mul_f32_e32 v25, v25, v24
	v_fmamk_f32 v24, v131, 0x3a000000, v7
	v_min_f32_e32 v24, 0x40e00000, v24
	v_mul_f32_e32 v27, 0x3fd9db23, v24
	v_mul_f32_e32 v27, 0xbfb8aa3b, v27
	v_fmamk_f32 v26, v99, 0x3a000000, v3
	v_exp_f32_e32 v27, v27
	v_med3_f32 v26, v26, s55, v199
	v_add_f32_e32 v26, 1.0, v26
	v_mul_f32_e32 v26, 4.0, v26
	v_mul_f32_e32 v24, v24, v26
	v_add_f32_e32 v26, 1.0, v27
	v_fmamk_f32 v27, v136, 0x3a000000, v16
	v_min_f32_e32 v27, 0x40e00000, v27
	v_mul_f32_e32 v29, 0x3fd9db23, v27
	v_mul_f32_e32 v29, 0xbfb8aa3b, v29
	v_rcp_f32_e32 v26, v26
	v_exp_f32_e32 v29, v29
	v_mul_f32_e32 v26, v26, v24
	v_fmamk_f32 v24, v104, 0x3a000000, v12
	v_add_f32_e32 v29, 1.0, v29
	v_med3_f32 v24, v24, s55, v199
	v_rcp_f32_e32 v29, v29
	v_add_f32_e32 v24, 1.0, v24
	v_mul_f32_e32 v24, 4.0, v24
	v_mul_f32_e32 v24, v27, v24
	v_mul_f32_e32 v27, v29, v24
	v_fmamk_f32 v24, v132, 0x3a000000, v8
	v_min_f32_e32 v24, 0x40e00000, v24
	v_mul_f32_e32 v30, 0x3fd9db23, v24
	v_mul_f32_e32 v30, 0xbfb8aa3b, v30
	v_fmamk_f32 v29, v100, 0x3a000000, v4
	v_exp_f32_e32 v30, v30
	v_med3_f32 v29, v29, s55, v199
	v_add_f32_e32 v29, 1.0, v29
	v_mul_f32_e32 v29, 4.0, v29
	v_mul_f32_e32 v24, v24, v29
	v_add_f32_e32 v29, 1.0, v30
	v_fmamk_f32 v30, v137, 0x3a000000, v17
	v_min_f32_e32 v30, 0x40e00000, v30
	v_mul_f32_e32 v31, 0x3fd9db23, v30
	v_mul_f32_e32 v31, 0xbfb8aa3b, v31
	v_rcp_f32_e32 v29, v29
	v_exp_f32_e32 v31, v31
	v_mul_f32_e32 v29, v29, v24
	v_fmamk_f32 v24, v105, 0x3a000000, v13
	v_add_f32_e32 v31, 1.0, v31
	v_med3_f32 v24, v24, s55, v199
	v_rcp_f32_e32 v31, v31
	v_add_f32_e32 v24, 1.0, v24
	v_mul_f32_e32 v24, 4.0, v24
	v_mul_f32_e32 v24, v30, v24
	v_mul_f32_e32 v30, v31, v24
	v_fmamk_f32 v24, v133, 0x3a000000, v9
	v_min_f32_e32 v24, 0x40e00000, v24
	v_mul_f32_e32 v32, 0x3fd9db23, v24
	v_mul_f32_e32 v32, 0xbfb8aa3b, v32
	v_fmamk_f32 v31, v101, 0x3a000000, v5
	v_exp_f32_e32 v32, v32
	v_med3_f32 v31, v31, s55, v199
	v_add_f32_e32 v31, 1.0, v31
	v_mul_f32_e32 v31, 4.0, v31
	v_mul_f32_e32 v31, v24, v31
	v_add_f32_e32 v24, 1.0, v32
	v_rcp_f32_e32 v32, v24
	v_mov_b32_e32 v24, v171
	v_cvt_pk_fp8_f32 v24, v23, v25
	v_ashrrev_i32_e32 v23, 31, v22
	v_lshlrev_b64 v[22:23], 11, v[22:23]
	v_mov_b32_e32 v25, v171
	v_lshl_add_u64 v[22:23], s[22:23], 0, v[22:23]
	v_cvt_pk_fp8_f32 v25, v28, v26
	v_lshl_add_u64 v[20:21], v[22:23], 0, v[20:21]
	v_fmamk_f32 v22, v94, 0x3a000000, v14
	v_min_f32_e32 v22, 0x40e00000, v22
	v_mul_f32_e32 v23, 0x3fd9db23, v22
	v_mul_f32_e32 v26, v32, v31
	v_mul_f32_e32 v23, 0xbfb8aa3b, v23
	v_cvt_pk_fp8_f32 v24, v27, v30 op_sel:[0,0,1]
	v_cvt_pk_fp8_f32 v25, v29, v26 op_sel:[0,0,1]
	v_exp_f32_e32 v23, v23
	global_store_dwordx2 v[20:21], v[24:25], off
	v_fmamk_f32 v20, v62, 0x3a000000, v10
	v_add_f32_e32 v21, 1.0, v23
	v_med3_f32 v20, v20, s55, v199
	v_rcp_f32_e32 v21, v21
	v_add_f32_e32 v20, 1.0, v20
	v_mul_f32_e32 v20, 4.0, v20
	v_mul_f32_e32 v20, v22, v20
	v_mul_f32_e32 v21, v21, v20
	v_fmamk_f32 v20, v90, 0x3a000000, v6
	v_min_f32_e32 v20, 0x40e00000, v20
	v_mul_f32_e32 v23, 0x3fd9db23, v20
	v_mul_f32_e32 v23, 0xbfb8aa3b, v23
	v_fmamk_f32 v22, v58, 0x3a000000, v2
	v_exp_f32_e32 v23, v23
	v_med3_f32 v22, v22, s55, v199
	v_add_f32_e32 v22, 1.0, v22
	v_mul_f32_e32 v22, 4.0, v22
	v_mul_f32_e32 v20, v20, v22
	v_add_f32_e32 v22, 1.0, v23
	v_fmamk_f32 v23, v95, 0x3a000000, v15
	v_min_f32_e32 v23, 0x40e00000, v23
	v_mul_f32_e32 v24, 0x3fd9db23, v23
	v_mul_f32_e32 v24, 0xbfb8aa3b, v24
	v_rcp_f32_e32 v22, v22
	v_exp_f32_e32 v24, v24
	v_mul_f32_e32 v22, v22, v20
	v_fmamk_f32 v20, v63, 0x3a000000, v11
	v_add_f32_e32 v24, 1.0, v24
	v_med3_f32 v20, v20, s55, v199
	v_rcp_f32_e32 v24, v24
	v_add_f32_e32 v20, 1.0, v20
; __device__ __forceinline__ unsigned pk4f8(float a, float b, float c, float d) { int r = 0; r = __builtin_amdgcn_cvt_pk_fp8_f32(a, b, r, false); r = __builtin_amdgcn_cvt_pk_fp8_f32(c, d, r, true); return (unsigned)r; }
; __device__ __forceinline__ float sigm(float x) { return __builtin_amdgcn_rcpf(1.f + __expf(-x)); }
;     __device__ __forceinline__ void operator()(const f32x4 (&acc)[2][2][4][2], const Unit& u, int wr, int wc, int fr, int fq) const {
;     ...
;             for (int m = 0; m < 4; ++m) { const size_t r = (size_t)(row0 + ai * HALF + m * 16);
;                 constexpr float DS = 1.f / (F8_SX * F8_SW);
;                 const f32x4 ga = acc[ai][0][m][0] * DS + bg0, gb = acc[ai][0][m][1] * DS + bg1, ua = acc[ai][1][m][0] * DS + bu0, ub = acc[ai][1][m][1] * DS + bu1;
;                 float o[8];
; #pragma unroll
;                 for (int j = 0; j < 4; ++j) { const float g = fminf(ga[j], 7.f), up = fminf(fmaxf(ua[j], -7.f), 7.f); o[j] = F8_SA * (up + 1.f) * g * sigm(1.702f * g);
;                                               const float g2 = fminf(gb[j], 7.f), up2 = fminf(fmaxf(ub[j], -7.f), 7.f); o[4 + j] = F8_SA * (up2 + 1.f) * g2 * sigm(1.702f * g2); }
;                 v2u w; w.x = pk4f8(o[0], o[1], o[2], o[3]); w.y = pk4f8(o[4], o[5], o[6], o[7]);
;                 *(v2u*)(ACT + r * FF + colg) = w; }
	v_mul_f32_e32 v20, 4.0, v20
	v_mul_f32_e32 v20, v23, v20
	v_mul_f32_e32 v23, v24, v20
	v_fmamk_f32 v20, v91, 0x3a000000, v7
	v_min_f32_e32 v20, 0x40e00000, v20
	v_mul_f32_e32 v25, 0x3fd9db23, v20
	v_mul_f32_e32 v25, 0xbfb8aa3b, v25
	v_fmamk_f32 v24, v59, 0x3a000000, v3
	v_exp_f32_e32 v25, v25
	v_med3_f32 v24, v24, s55, v199
	v_add_f32_e32 v24, 1.0, v24
	v_mul_f32_e32 v24, 4.0, v24
	v_mul_f32_e32 v20, v20, v24
	v_add_f32_e32 v24, 1.0, v25
	v_fmamk_f32 v25, v96, 0x3a000000, v16
	v_min_f32_e32 v25, 0x40e00000, v25
	v_mul_f32_e32 v26, 0x3fd9db23, v25
	v_mul_f32_e32 v26, 0xbfb8aa3b, v26
	v_rcp_f32_e32 v24, v24
	v_exp_f32_e32 v26, v26
	v_mul_f32_e32 v24, v24, v20
	v_fmamk_f32 v20, v64, 0x3a000000, v12
	v_add_f32_e32 v26, 1.0, v26
	v_med3_f32 v20, v20, s55, v199
	v_rcp_f32_e32 v26, v26
	v_add_f32_e32 v20, 1.0, v20
	v_mul_f32_e32 v20, 4.0, v20
	v_mul_f32_e32 v20, v25, v20
	v_mul_f32_e32 v25, v26, v20
	v_fmamk_f32 v20, v92, 0x3a000000, v8
	v_min_f32_e32 v20, 0x40e00000, v20
	v_mul_f32_e32 v27, 0x3fd9db23, v20
	v_mul_f32_e32 v27, 0xbfb8aa3b, v27
	v_fmamk_f32 v26, v60, 0x3a000000, v4
	v_exp_f32_e32 v27, v27
	v_med3_f32 v26, v26, s55, v199
	v_add_f32_e32 v26, 1.0, v26
	v_mul_f32_e32 v26, 4.0, v26
	v_mul_f32_e32 v20, v20, v26
	v_add_f32_e32 v26, 1.0, v27
	v_fmamk_f32 v27, v97, 0x3a000000, v17
	v_min_f32_e32 v27, 0x40e00000, v27
	v_mul_f32_e32 v28, 0x3fd9db23, v27
	v_mul_f32_e32 v28, 0xbfb8aa3b, v28
	v_rcp_f32_e32 v26, v26
	v_exp_f32_e32 v28, v28
	v_mul_f32_e32 v26, v26, v20
	v_fmamk_f32 v20, v65, 0x3a000000, v13
	v_add_f32_e32 v28, 1.0, v28
	v_med3_f32 v20, v20, s55, v199
	v_rcp_f32_e32 v28, v28
	v_add_f32_e32 v20, 1.0, v20
	v_mul_f32_e32 v20, 4.0, v20
	v_mul_f32_e32 v20, v27, v20
	v_mul_f32_e32 v27, v28, v20
	v_fmamk_f32 v20, v93, 0x3a000000, v9
	v_min_f32_e32 v28, 0x40e00000, v20
	v_mul_f32_e32 v29, 0x3fd9db23, v28
	v_mul_f32_e32 v29, 0xbfb8aa3b, v29
	v_exp_f32_e32 v29, v29
	v_fmamk_f32 v20, v61, 0x3a000000, v5
	v_med3_f32 v20, v20, s55, v199
	v_add_f32_e32 v20, 1.0, v20
	v_mul_f32_e32 v30, 4.0, v20
	v_add_f32_e32 v20, 1.0, v29
	v_rcp_f32_e32 v29, v20
	v_mov_b32_e32 v20, v171
	v_cvt_pk_fp8_f32 v20, v21, v23
	v_mov_b32_e32 v21, v171
	v_cvt_pk_fp8_f32 v21, v22, v24
	v_fmamk_f32 v24, v86, 0x3a000000, v14
	v_min_f32_e32 v24, 0x40e00000, v24
	v_mul_f32_e32 v22, v28, v30
	v_cvt_pk_fp8_f32 v20, v25, v27 op_sel:[0,0,1]
	v_mul_f32_e32 v25, 0x3fd9db23, v24
	v_mul_f32_e32 v22, v29, v22
	v_mul_f32_e32 v25, 0xbfb8aa3b, v25
	v_cvt_pk_fp8_f32 v21, v26, v22 op_sel:[0,0,1]
	v_exp_f32_e32 v25, v25
	v_add_co_u32_e32 v22, vcc, s56, v18
	s_nop 1
	v_addc_co_u32_e32 v23, vcc, 0, v19, vcc
	global_store_dwordx2 v[22:23], v[20:21], off
	v_fmamk_f32 v20, v54, 0x3a000000, v10
	v_add_f32_e32 v21, 1.0, v25
	v_med3_f32 v20, v20, s55, v199
	v_rcp_f32_e32 v21, v21
	v_add_f32_e32 v20, 1.0, v20
	v_mul_f32_e32 v20, 4.0, v20
	v_mul_f32_e32 v20, v24, v20
	v_mul_f32_e32 v21, v21, v20
	v_fmamk_f32 v20, v82, 0x3a000000, v6
	v_min_f32_e32 v20, 0x40e00000, v20
	v_mul_f32_e32 v23, 0x3fd9db23, v20
	v_mul_f32_e32 v23, 0xbfb8aa3b, v23
	v_fmamk_f32 v22, v50, 0x3a000000, v2
	v_exp_f32_e32 v23, v23
	v_med3_f32 v22, v22, s55, v199
	v_add_f32_e32 v22, 1.0, v22
	v_mul_f32_e32 v22, 4.0, v22
	v_mul_f32_e32 v20, v20, v22
	v_add_f32_e32 v22, 1.0, v23
	v_fmamk_f32 v23, v87, 0x3a000000, v15
	v_min_f32_e32 v23, 0x40e00000, v23
	v_mul_f32_e32 v24, 0x3fd9db23, v23
	v_mul_f32_e32 v24, 0xbfb8aa3b, v24
	v_rcp_f32_e32 v22, v22
	v_exp_f32_e32 v24, v24
	v_mul_f32_e32 v22, v22, v20
	v_fmamk_f32 v20, v55, 0x3a000000, v11
	v_add_f32_e32 v24, 1.0, v24
	v_med3_f32 v20, v20, s55, v199
	v_rcp_f32_e32 v24, v24
	v_add_f32_e32 v20, 1.0, v20
	v_mul_f32_e32 v20, 4.0, v20
	v_mul_f32_e32 v20, v23, v20
	v_mul_f32_e32 v23, v24, v20
	v_fmamk_f32 v20, v83, 0x3a000000, v7
	v_min_f32_e32 v20, 0x40e00000, v20
	v_mul_f32_e32 v25, 0x3fd9db23, v20
	v_mul_f32_e32 v25, 0xbfb8aa3b, v25
	v_fmamk_f32 v24, v51, 0x3a000000, v3
	v_exp_f32_e32 v25, v25
	v_med3_f32 v24, v24, s55, v199
	v_add_f32_e32 v24, 1.0, v24
	v_mul_f32_e32 v24, 4.0, v24
	v_mul_f32_e32 v20, v20, v24
	v_add_f32_e32 v24, 1.0, v25
	v_fmamk_f32 v25, v88, 0x3a000000, v16
	v_min_f32_e32 v25, 0x40e00000, v25
	v_mul_f32_e32 v26, 0x3fd9db23, v25
	v_mul_f32_e32 v26, 0xbfb8aa3b, v26
	v_rcp_f32_e32 v24, v24
	v_exp_f32_e32 v26, v26
	v_mul_f32_e32 v24, v24, v20
	v_fmamk_f32 v20, v56, 0x3a000000, v12
	v_add_f32_e32 v26, 1.0, v26
	v_med3_f32 v20, v20, s55, v199
	v_rcp_f32_e32 v26, v26
	v_add_f32_e32 v20, 1.0, v20
	v_mul_f32_e32 v20, 4.0, v20
	v_mul_f32_e32 v20, v25, v20
	v_mul_f32_e32 v25, v26, v20
	v_fmamk_f32 v20, v84, 0x3a000000, v8
	v_min_f32_e32 v20, 0x40e00000, v20
	v_mul_f32_e32 v27, 0x3fd9db23, v20
	v_mul_f32_e32 v27, 0xbfb8aa3b, v27
	v_fmamk_f32 v26, v52, 0x3a000000, v4
	v_exp_f32_e32 v27, v27
	v_med3_f32 v26, v26, s55, v199
	v_add_f32_e32 v26, 1.0, v26
	v_mul_f32_e32 v26, 4.0, v26
	v_mul_f32_e32 v20, v20, v26
	v_add_f32_e32 v26, 1.0, v27
	v_fmamk_f32 v27, v89, 0x3a000000, v17
	v_min_f32_e32 v27, 0x40e00000, v27
	v_mul_f32_e32 v28, 0x3fd9db23, v27
	v_mul_f32_e32 v28, 0xbfb8aa3b, v28
	v_rcp_f32_e32 v26, v26
	v_exp_f32_e32 v28, v28
	v_mul_f32_e32 v26, v26, v20
	v_fmamk_f32 v20, v57, 0x3a000000, v13
	v_add_f32_e32 v28, 1.0, v28
	v_med3_f32 v20, v20, s55, v199
	v_rcp_f32_e32 v28, v28
	v_add_f32_e32 v20, 1.0, v20
	v_mul_f32_e32 v20, 4.0, v20
	v_mul_f32_e32 v20, v27, v20
	v_mul_f32_e32 v27, v28, v20
	v_fmamk_f32 v20, v85, 0x3a000000, v9
	v_min_f32_e32 v28, 0x40e00000, v20
	v_mul_f32_e32 v29, 0x3fd9db23, v28
	v_mul_f32_e32 v29, 0xbfb8aa3b, v29
	v_exp_f32_e32 v29, v29
	v_fmamk_f32 v20, v53, 0x3a000000, v5
	v_med3_f32 v20, v20, s55, v199
	v_add_f32_e32 v20, 1.0, v20
	v_mul_f32_e32 v30, 4.0, v20
; __device__ __forceinline__ unsigned pk4f8(float a, float b, float c, float d) { int r = 0; r = __builtin_amdgcn_cvt_pk_fp8_f32(a, b, r, false); r = __builtin_amdgcn_cvt_pk_fp8_f32(c, d, r, true); return (unsigned)r; }
; __device__ __forceinline__ float sigm(float x) { return __builtin_amdgcn_rcpf(1.f + __expf(-x)); }
;     __device__ __forceinline__ void operator()(const f32x4 (&acc)[2][2][4][2], const Unit& u, int wr, int wc, int fr, int fq) const {
;     ...
;             for (int m = 0; m < 4; ++m) { const size_t r = (size_t)(row0 + ai * HALF + m * 16);
;                 constexpr float DS = 1.f / (F8_SX * F8_SW);
;                 const f32x4 ga = acc[ai][0][m][0] * DS + bg0, gb = acc[ai][0][m][1] * DS + bg1, ua = acc[ai][1][m][0] * DS + bu0, ub = acc[ai][1][m][1] * DS + bu1;
;                 float o[8];
; #pragma unroll
;                 for (int j = 0; j < 4; ++j) { const float g = fminf(ga[j], 7.f), up = fminf(fmaxf(ua[j], -7.f), 7.f); o[j] = F8_SA * (up + 1.f) * g * sigm(1.702f * g);
;                                               const float g2 = fminf(gb[j], 7.f), up2 = fminf(fmaxf(ub[j], -7.f), 7.f); o[4 + j] = F8_SA * (up2 + 1.f) * g2 * sigm(1.702f * g2); }
;                 v2u w; w.x = pk4f8(o[0], o[1], o[2], o[3]); w.y = pk4f8(o[4], o[5], o[6], o[7]);
;                 *(v2u*)(ACT + r * FF + colg) = w; }
	v_add_f32_e32 v20, 1.0, v29
	v_rcp_f32_e32 v29, v20
	v_mov_b32_e32 v20, v171
	v_cvt_pk_fp8_f32 v20, v21, v23
	v_mov_b32_e32 v21, v171
	v_cvt_pk_fp8_f32 v21, v22, v24
	v_fmamk_f32 v24, v78, 0x3a000000, v14
	v_min_f32_e32 v24, 0x40e00000, v24
	v_mul_f32_e32 v22, v28, v30
	v_cvt_pk_fp8_f32 v20, v25, v27 op_sel:[0,0,1]
	v_mul_f32_e32 v25, 0x3fd9db23, v24
	v_mul_f32_e32 v22, v29, v22
	v_mul_f32_e32 v25, 0xbfb8aa3b, v25
	v_cvt_pk_fp8_f32 v21, v26, v22 op_sel:[0,0,1]
	v_exp_f32_e32 v25, v25
	v_add_co_u32_e32 v22, vcc, s57, v18
	v_fmamk_f32 v14, v70, 0x3a000000, v14
	s_nop 0
	v_addc_co_u32_e32 v23, vcc, 0, v19, vcc
	global_store_dwordx2 v[22:23], v[20:21], off
	v_fmamk_f32 v20, v46, 0x3a000000, v10
	v_add_f32_e32 v21, 1.0, v25
	v_med3_f32 v20, v20, s55, v199
	v_rcp_f32_e32 v21, v21
	v_add_f32_e32 v20, 1.0, v20
	v_mul_f32_e32 v20, 4.0, v20
	v_mul_f32_e32 v20, v24, v20
	v_mul_f32_e32 v21, v21, v20
	v_fmamk_f32 v20, v74, 0x3a000000, v6
	v_min_f32_e32 v20, 0x40e00000, v20
	v_mul_f32_e32 v23, 0x3fd9db23, v20
	v_mul_f32_e32 v23, 0xbfb8aa3b, v23
	v_fmamk_f32 v22, v42, 0x3a000000, v2
	v_exp_f32_e32 v23, v23
	v_med3_f32 v22, v22, s55, v199
	v_add_f32_e32 v22, 1.0, v22
	v_mul_f32_e32 v22, 4.0, v22
	v_mul_f32_e32 v20, v20, v22
	v_add_f32_e32 v22, 1.0, v23
	v_fmamk_f32 v23, v79, 0x3a000000, v15
	v_min_f32_e32 v23, 0x40e00000, v23
	v_mul_f32_e32 v24, 0x3fd9db23, v23
	v_mul_f32_e32 v24, 0xbfb8aa3b, v24
	v_rcp_f32_e32 v22, v22
	v_exp_f32_e32 v24, v24
	v_fmamk_f32 v10, v38, 0x3a000000, v10
	v_med3_f32 v10, v10, s55, v199
	v_mul_f32_e32 v22, v22, v20
	v_fmamk_f32 v20, v47, 0x3a000000, v11
	v_add_f32_e32 v24, 1.0, v24
	v_med3_f32 v20, v20, s55, v199
	v_rcp_f32_e32 v24, v24
	v_add_f32_e32 v20, 1.0, v20
	v_mul_f32_e32 v20, 4.0, v20
	v_mul_f32_e32 v20, v23, v20
	v_mul_f32_e32 v23, v24, v20
	v_fmamk_f32 v20, v75, 0x3a000000, v7
	v_min_f32_e32 v20, 0x40e00000, v20
	v_mul_f32_e32 v25, 0x3fd9db23, v20
	v_mul_f32_e32 v25, 0xbfb8aa3b, v25
	v_fmamk_f32 v24, v43, 0x3a000000, v3
	v_exp_f32_e32 v25, v25
	v_med3_f32 v24, v24, s55, v199
	v_add_f32_e32 v24, 1.0, v24
	v_mul_f32_e32 v24, 4.0, v24
	v_mul_f32_e32 v20, v20, v24
	v_add_f32_e32 v24, 1.0, v25
	v_fmamk_f32 v25, v80, 0x3a000000, v16
	v_min_f32_e32 v25, 0x40e00000, v25
	v_mul_f32_e32 v26, 0x3fd9db23, v25
	v_mul_f32_e32 v26, 0xbfb8aa3b, v26
	v_rcp_f32_e32 v24, v24
	v_exp_f32_e32 v26, v26
	v_add_f32_e32 v10, 1.0, v10
	v_fmamk_f32 v6, v66, 0x3a000000, v6
	v_mul_f32_e32 v24, v24, v20
	v_fmamk_f32 v20, v48, 0x3a000000, v12
	v_add_f32_e32 v26, 1.0, v26
	v_med3_f32 v20, v20, s55, v199
	v_rcp_f32_e32 v26, v26
	v_add_f32_e32 v20, 1.0, v20
	v_mul_f32_e32 v20, 4.0, v20
	v_mul_f32_e32 v20, v25, v20
	v_mul_f32_e32 v25, v26, v20
	v_fmamk_f32 v20, v76, 0x3a000000, v8
	v_min_f32_e32 v20, 0x40e00000, v20
	v_mul_f32_e32 v27, 0x3fd9db23, v20
	v_mul_f32_e32 v27, 0xbfb8aa3b, v27
	v_fmamk_f32 v26, v44, 0x3a000000, v4
	v_exp_f32_e32 v27, v27
	v_med3_f32 v26, v26, s55, v199
	v_add_f32_e32 v26, 1.0, v26
	v_mul_f32_e32 v26, 4.0, v26
	v_mul_f32_e32 v20, v20, v26
	v_add_f32_e32 v26, 1.0, v27
	v_fmamk_f32 v27, v81, 0x3a000000, v17
	v_min_f32_e32 v27, 0x40e00000, v27
	v_mul_f32_e32 v28, 0x3fd9db23, v27
	v_mul_f32_e32 v28, 0xbfb8aa3b, v28
	v_rcp_f32_e32 v26, v26
	v_exp_f32_e32 v28, v28
	v_min_f32_e32 v14, 0x40e00000, v14
	v_mul_f32_e32 v10, 4.0, v10
	v_mul_f32_e32 v26, v26, v20
	v_fmamk_f32 v20, v49, 0x3a000000, v13
	v_add_f32_e32 v28, 1.0, v28
	v_med3_f32 v20, v20, s55, v199
	v_rcp_f32_e32 v28, v28
	v_add_f32_e32 v20, 1.0, v20
	v_mul_f32_e32 v20, 4.0, v20
	v_mul_f32_e32 v20, v27, v20
	v_mul_f32_e32 v27, v28, v20
	v_fmamk_f32 v20, v77, 0x3a000000, v9
	v_min_f32_e32 v28, 0x40e00000, v20
	v_mul_f32_e32 v29, 0x3fd9db23, v28
	v_mul_f32_e32 v29, 0xbfb8aa3b, v29
	v_exp_f32_e32 v29, v29
	v_fmamk_f32 v20, v45, 0x3a000000, v5
	v_med3_f32 v20, v20, s55, v199
	v_add_f32_e32 v20, 1.0, v20
; #define PG8_BAR __builtin_amdgcn_s_barrier()
; __device__ __forceinline__ unsigned pk4f8(float a, float b, float c, float d) { int r = 0; r = __builtin_amdgcn_cvt_pk_fp8_f32(a, b, r, false); r = __builtin_amdgcn_cvt_pk_fp8_f32(c, d, r, true); return (unsigned)r; }
; __device__ __forceinline__ float sigm(float x) { return __builtin_amdgcn_rcpf(1.f + __expf(-x)); }
; template <class Epi, class Sched, bool ALIGN_EPI = false, bool SP2 = false, bool FP8 = false, bool I8 = false>
; __device__ __forceinline__ void gemm_phase(PG8_LAS unsigned char* lds, const Gemm g, const Sched& S, const Epi& E) {
;     ...
;         if (!has_next) break;
; #pragma unroll
;         for (int a = 0; a < 2; ++a)
; #pragma unroll
;             for (int b = 0; b < 2; ++b)
; #pragma unroll
;                 for (int m = 0; m < 4; ++m)
; #pragma unroll
;                     for (int n = 0; n < 2; ++n) acc[a][b][m][n] = (f32x4){0.f, 0.f, 0.f, 0.f};
;         cur = nxt; cA = nA; cB = nB; ++ui;
;         if constexpr (ALIGN_EPI) { if (wr == 1) PG8_BAR; }
;     __device__ __forceinline__ void operator()(const f32x4 (&acc)[2][2][4][2], const Unit& u, int wr, int wc, int fr, int fq) const {
;     ...
;             for (int m = 0; m < 4; ++m) { const size_t r = (size_t)(row0 + ai * HALF + m * 16);
;                 constexpr float DS = 1.f / (F8_SX * F8_SW);
;                 const f32x4 ga = acc[ai][0][m][0] * DS + bg0, gb = acc[ai][0][m][1] * DS + bg1, ua = acc[ai][1][m][0] * DS + bu0, ub = acc[ai][1][m][1] * DS + bu1;
;                 float o[8];
; #pragma unroll
;                 for (int j = 0; j < 4; ++j) { const float g = fminf(ga[j], 7.f), up = fminf(fmaxf(ua[j], -7.f), 7.f); o[j] = F8_SA * (up + 1.f) * g * sigm(1.702f * g);
;                                               const float g2 = fminf(gb[j], 7.f), up2 = fminf(fmaxf(ub[j], -7.f), 7.f); o[4 + j] = F8_SA * (up2 + 1.f) * g2 * sigm(1.702f * g2); }
;                 v2u w; w.x = pk4f8(o[0], o[1], o[2], o[3]); w.y = pk4f8(o[4], o[5], o[6], o[7]);
;                 *(v2u*)(ACT + r * FF + colg) = w; }
	v_mul_f32_e32 v30, 4.0, v20
	v_add_f32_e32 v20, 1.0, v29
	v_rcp_f32_e32 v29, v20
	v_mov_b32_e32 v20, v171
	v_cvt_pk_fp8_f32 v20, v21, v23
	v_mov_b32_e32 v21, v171
	v_min_f32_e32 v6, 0x40e00000, v6
	v_cvt_pk_fp8_f32 v21, v22, v24
	v_mul_f32_e32 v24, 0x3fd9db23, v14
	v_mul_f32_e32 v10, v14, v10
	v_mul_f32_e32 v14, 0x3fd9db23, v6
	v_mul_f32_e32 v14, 0xbfb8aa3b, v14
	v_fmamk_f32 v2, v34, 0x3a000000, v2
	v_exp_f32_e32 v14, v14
	v_med3_f32 v2, v2, s55, v199
	v_add_f32_e32 v2, 1.0, v2
	v_mul_f32_e32 v2, 4.0, v2
	v_mul_f32_e32 v2, v6, v2
	v_add_f32_e32 v6, 1.0, v14
	v_fmamk_f32 v14, v71, 0x3a000000, v15
	v_min_f32_e32 v14, 0x40e00000, v14
	v_mul_f32_e32 v15, 0x3fd9db23, v14
	v_mul_f32_e32 v15, 0xbfb8aa3b, v15
	v_rcp_f32_e32 v6, v6
	v_exp_f32_e32 v15, v15
	v_fmamk_f32 v3, v35, 0x3a000000, v3
	v_med3_f32 v3, v3, s55, v199
	v_mul_f32_e32 v6, v6, v2
	v_fmamk_f32 v2, v39, 0x3a000000, v11
	v_add_f32_e32 v11, 1.0, v15
	v_med3_f32 v2, v2, s55, v199
	v_rcp_f32_e32 v11, v11
	v_add_f32_e32 v2, 1.0, v2
	v_mul_f32_e32 v2, 4.0, v2
	v_mul_f32_e32 v2, v14, v2
	v_mul_f32_e32 v11, v11, v2
	v_fmamk_f32 v2, v67, 0x3a000000, v7
	v_min_f32_e32 v2, 0x40e00000, v2
	v_mul_f32_e32 v7, 0x3fd9db23, v2
	v_mul_f32_e32 v7, 0xbfb8aa3b, v7
	v_exp_f32_e32 v7, v7
	v_add_f32_e32 v3, 1.0, v3
	v_mul_f32_e32 v3, 4.0, v3
	v_mul_f32_e32 v2, v2, v3
	v_add_f32_e32 v3, 1.0, v7
	v_fmamk_f32 v7, v72, 0x3a000000, v16
	v_min_f32_e32 v7, 0x40e00000, v7
	v_mul_f32_e32 v14, 0x3fd9db23, v7
	v_mul_f32_e32 v14, 0xbfb8aa3b, v14
	v_rcp_f32_e32 v3, v3
	v_exp_f32_e32 v14, v14
	v_fmac_f32_e32 v17, 0x3a000000, v73
	v_fmac_f32_e32 v13, 0x3a000000, v41
	v_mul_f32_e32 v15, v3, v2
	v_fmamk_f32 v2, v40, 0x3a000000, v12
	v_add_f32_e32 v3, 1.0, v14
	v_med3_f32 v2, v2, s55, v199
	v_rcp_f32_e32 v3, v3
	v_add_f32_e32 v2, 1.0, v2
	v_mul_f32_e32 v2, 4.0, v2
	v_mul_f32_e32 v2, v7, v2
	v_mul_f32_e32 v7, v3, v2
	v_fmamk_f32 v2, v68, 0x3a000000, v8
	v_min_f32_e32 v2, 0x40e00000, v2
	v_fmamk_f32 v3, v36, 0x3a000000, v4
	v_mul_f32_e32 v4, 0x3fd9db23, v2
	v_mul_f32_e32 v4, 0xbfb8aa3b, v4
	v_exp_f32_e32 v4, v4
	v_med3_f32 v3, v3, s55, v199
	v_add_f32_e32 v3, 1.0, v3
	v_mul_f32_e32 v3, 4.0, v3
	v_mul_f32_e32 v2, v2, v3
	v_add_f32_e32 v3, 1.0, v4
	v_min_f32_e32 v4, 0x40e00000, v17
	v_mul_f32_e32 v8, 0x3fd9db23, v4
	v_mul_f32_e32 v8, 0xbfb8aa3b, v8
	v_rcp_f32_e32 v3, v3
	v_exp_f32_e32 v8, v8
	v_mul_f32_e32 v22, v28, v30
	v_mul_f32_e32 v22, v29, v22
	v_mul_f32_e32 v12, v3, v2
	v_add_f32_e32 v3, 1.0, v8
	v_med3_f32 v2, v13, s55, v199
	v_rcp_f32_e32 v3, v3
	v_mul_f32_e32 v24, 0xbfb8aa3b, v24
	v_add_f32_e32 v2, 1.0, v2
	v_cvt_pk_fp8_f32 v20, v25, v27 op_sel:[0,0,1]
	v_cvt_pk_fp8_f32 v21, v26, v22 op_sel:[0,0,1]
	v_exp_f32_e32 v24, v24
	v_mul_f32_e32 v2, 4.0, v2
	v_fmac_f32_e32 v9, 0x3a000000, v69
	v_mul_f32_e32 v2, v4, v2
	v_min_f32_e32 v8, 0x40e00000, v9
	v_add_co_u32_e32 v22, vcc, s58, v18
	v_mul_f32_e32 v4, v3, v2
	v_mul_f32_e32 v2, 0x3fd9db23, v8
	v_addc_co_u32_e32 v23, vcc, 0, v19, vcc
	v_mul_f32_e32 v2, 0xbfb8aa3b, v2
	global_store_dwordx2 v[22:23], v[20:21], off
	v_add_f32_e32 v20, 1.0, v24
	v_exp_f32_e32 v2, v2
	v_rcp_f32_e32 v20, v20
	v_fmac_f32_e32 v5, 0x3a000000, v37
	v_med3_f32 v3, v5, s55, v199
	v_add_f32_e32 v3, 1.0, v3
	v_add_f32_e32 v2, 1.0, v2
	v_mul_f32_e32 v10, v20, v10
	v_mul_f32_e32 v5, 4.0, v3
	v_rcp_f32_e32 v9, v2
	v_mov_b32_e32 v2, v171
	v_mov_b32_e32 v3, v171
	v_cvt_pk_fp8_f32 v2, v10, v11
	v_cvt_pk_fp8_f32 v3, v6, v15
	v_mul_f32_e32 v5, v8, v5
	v_mul_f32_e32 v5, v9, v5
	v_cvt_pk_fp8_f32 v2, v7, v4 op_sel:[0,0,1]
	v_cvt_pk_fp8_f32 v3, v12, v5 op_sel:[0,0,1]
	v_add_co_u32_e32 v4, vcc, 0x58000, v18
	s_nop 1
	v_addc_co_u32_e32 v5, vcc, 0, v19, vcc
	s_and_b64 vcc, exec, s[6:7]
	global_store_dwordx2 v[4:5], v[2:3], off
	s_cbranch_vccnz .LBB0_1925
	s_andn2_b64 vcc, exec, s[20:21]
	s_cbranch_vccnz .LBB0_1911
	s_barrier
	s_branch .LBB0_1911

; __device__ __forceinline__ unsigned pk4f8(float a, float b, float c, float d) { int r = 0; r = __builtin_amdgcn_cvt_pk_fp8_f32(a, b, r, false); r = __builtin_amdgcn_cvt_pk_fp8_f32(c, d, r, true); return (unsigned)r; }
;     __device__ __forceinline__ void operator()(const f32x4 (&acc)[2][2][4][2], const Unit& u, int wr, int wc, int fr, int fq) const {
;         const int e = tile_e[u.pm]; const int col0 = u.pn * BM + wc * 32 + 8 * fq;
;         const float* bp = bdn + (size_t)e * D + col0; constexpr float DS = 1.f / (F8_SA * F8_SW);
; #pragma unroll
;         for (int bj = 0; bj < 2; ++bj) { const f32x4 b0 = *(const f32x4*)(bp + bj * HALF), b1 = *(const f32x4*)(bp + bj * HALF + 4);
; #pragma unroll
;             for (int ai = 0; ai < 2; ++ai)
; #pragma unroll
;                 for (int m = 0; m < 4; ++m) { const int r = u.ord * 256 + ai * HALF + wr * 64 + m * 16 + fr;
;                     const int dst = rowdst[r]; const float w = rowwt[r];
;                     const f32x4 v0 = (acc[ai][bj][m][0] * DS + b0) * (w * F8_SY), v1 = (acc[ai][bj][m][1] * DS + b1) * (w * F8_SY);
;                     v2u o; o.x = pk4f8(v0[0], v0[1], v0[2], v0[3]); o.y = pk4f8(v1[0], v1[1], v1[2], v1[3]);
;                     *(v2u*)(YS + (size_t)dst * D + col0 + bj * HALF) = o; } }
.LBB0_2400:
	s_lshl_b32 s6, s26, 2
	s_add_i32 s6, s6, 0
	s_add_i32 s6, s6, 0x20100
	v_mov_b32_e32 v0, s6
	s_lshl_b32 s6, s49, 8
	v_add_lshl_u32 v1, s6, v184, 2
	v_add_lshl_u32 v3, s6, v185, 2
	s_nop 15
	s_nop 15
	v_add_u32_e32 v23, s45, v1
	v_add_u32_e32 v181, s46, v1
	v_add_u32_e32 v1, s46, v3
	v_add_lshl_u32 v2, s6, v186, 2
	v_add_lshl_u32 v6, s6, v187, 2
	v_add_u32_e32 v4, s45, v2
	v_add_u32_e32 v5, s46, v2
	v_add_u32_e32 v7, s45, v6
	ds_read_b32 v0, v0
	ds_read_b32 v8, v1
	ds_read_b32 v2, v4
	ds_read_b32 v9, v5
	ds_read_b32 v20, v7
	ds_read_b32 v22, v23 offset:704
	ds_read_b32 v183, v181 offset:704
	s_waitcnt lgkmcnt(0)
	v_ashrrev_i32_e32 v1, 31, v0
	v_lshl_or_b32 v24, s24, 8, v188
	v_lshlrev_b64 v[0:1], 13, v[0:1]
	v_lshl_add_u64 v[0:1], s[84:85], 0, v[0:1]
	v_ashrrev_i32_e32 v25, 31, v24
	v_lshl_add_u64 v[26:27], v[24:25], 2, v[0:1]
	global_load_dwordx4 v[12:15], v[26:27], off
	global_load_dwordx4 v[16:19], v[26:27], off offset:16
	global_load_dwordx4 v[238:241], v[26:27], off offset:512
	global_load_dwordx4 v[242:245], v[26:27], off offset:528
	v_add_u32_e32 v0, s45, v3
	v_add_u32_e32 v1, s46, v6
	ds_read_b32 v0, v0
	ds_read_b32 v10, v1
	ds_read2st64_b32 v[4:5], v23 offset1:2
	ds_read2st64_b32 v[178:179], v181 offset1:2
	v_ashrrev_i32_e32 v3, 31, v2
	v_lshlrev_b64 v[2:3], 11, v[2:3]
	v_lshl_add_u64 v[2:3], s[2:3], 0, v[2:3]
	s_waitcnt lgkmcnt(0)
	v_ashrrev_i32_e32 v7, 31, v4
	v_mov_b32_e32 v6, v4
	v_mul_f32_e32 v178, 0x41800000, v178
	v_mul_f32_e32 v4, 0x41800000, v10
	v_lshl_add_u64 v[10:11], v[2:3], 0, v[24:25]
	v_mov_b32_e32 v28, 0
	v_mov_b32_e32 v29, 0
	v_ashrrev_i32_e32 v1, 31, v0
	v_mul_f32_e32 v180, 0x41800000, v8
	v_mov_b32_e32 v30, 0
	v_mov_b32_e32 v31, 0
	v_mul_f32_e32 v182, 0x41800000, v9
	v_lshlrev_b64 v[0:1], 11, v[0:1]
	v_mov_b32_e32 v176, 0
	v_mov_b32_e32 v177, 0
	v_lshl_add_u64 v[0:1], s[2:3], 0, v[0:1]
	v_lshl_add_u64 v[8:9], v[0:1], 0, v[24:25]
	v_lshlrev_b64 v[6:7], 11, v[6:7]
	v_lshl_add_u64 v[6:7], s[2:3], 0, v[6:7]
	v_lshl_add_u64 v[6:7], v[6:7], 0, v[24:25]
	v_ashrrev_i32_e32 v21, 31, v20
	s_and_b64 vcc, exec, s[4:5]
	s_mov_b64 s[4:5], -1
	s_waitcnt vmcnt(0)
	v_pk_fma_f32 v[2:3], v[156:157], s[14:15], v[12:13] op_sel_hi:[1,0,1]
	v_pk_fma_f32 v[152:153], v[152:153], s[14:15], v[16:17] op_sel_hi:[1,0,1]
	v_pk_fma_f32 v[148:149], v[148:149], s[14:15], v[12:13] op_sel_hi:[1,0,1]
	v_pk_fma_f32 v[144:145], v[144:145], s[14:15], v[16:17] op_sel_hi:[1,0,1]
	v_pk_mul_f32 v[2:3], v[2:3], v[178:179] op_sel_hi:[1,0]
	v_pk_mul_f32 v[152:153], v[152:153], v[178:179] op_sel_hi:[1,0]
	v_pk_fma_f32 v[140:141], v[140:141], s[14:15], v[12:13] op_sel_hi:[1,0,1]
	v_pk_fma_f32 v[136:137], v[136:137], s[14:15], v[16:17] op_sel_hi:[1,0,1]
	v_pk_mul_f32 v[148:149], v[148:149], v[180:181] op_sel_hi:[1,0]
	v_pk_mul_f32 v[144:145], v[144:145], v[180:181] op_sel_hi:[1,0]
	v_cvt_pk_fp8_f32 v28, v2, v3
	v_cvt_pk_fp8_f32 v29, v152, v153
	v_pk_mul_f32 v[140:141], v[140:141], v[182:183] op_sel_hi:[1,0]
	v_pk_mul_f32 v[136:137], v[136:137], v[182:183] op_sel_hi:[1,0]
	v_cvt_pk_fp8_f32 v30, v148, v149
	v_cvt_pk_fp8_f32 v31, v144, v145
	v_pk_fma_f32 v[0:1], v[158:159], s[14:15], v[14:15] op_sel_hi:[1,0,1]
	v_pk_fma_f32 v[154:155], v[154:155], s[14:15], v[18:19] op_sel_hi:[1,0,1]
	v_cvt_pk_fp8_f32 v176, v140, v141
	v_cvt_pk_fp8_f32 v177, v136, v137
	v_pk_fma_f32 v[150:151], v[150:151], s[14:15], v[14:15] op_sel_hi:[1,0,1]
	v_pk_fma_f32 v[146:147], v[146:147], s[14:15], v[18:19] op_sel_hi:[1,0,1]
	v_pk_mul_f32 v[0:1], v[0:1], v[178:179] op_sel_hi:[1,0]
	v_pk_mul_f32 v[154:155], v[154:155], v[178:179] op_sel_hi:[1,0]
	v_pk_fma_f32 v[142:143], v[142:143], s[14:15], v[14:15] op_sel_hi:[1,0,1]
	v_pk_fma_f32 v[138:139], v[138:139], s[14:15], v[18:19] op_sel_hi:[1,0,1]
	v_pk_mul_f32 v[150:151], v[150:151], v[180:181] op_sel_hi:[1,0]
	v_pk_mul_f32 v[146:147], v[146:147], v[180:181] op_sel_hi:[1,0]
	v_cvt_pk_fp8_f32 v28, v0, v1 op_sel:[0,0,1]
	v_cvt_pk_fp8_f32 v29, v154, v155 op_sel:[0,0,1]
	v_pk_mul_f32 v[142:143], v[142:143], v[182:183] op_sel_hi:[1,0]
	v_pk_mul_f32 v[138:139], v[138:139], v[182:183] op_sel_hi:[1,0]
	v_cvt_pk_fp8_f32 v30, v150, v151 op_sel:[0,0,1]
	v_cvt_pk_fp8_f32 v31, v146, v147 op_sel:[0,0,1]
	v_cvt_pk_fp8_f32 v176, v142, v143 op_sel:[0,0,1]
	v_cvt_pk_fp8_f32 v177, v138, v139 op_sel:[0,0,1]
	v_pk_fma_f32 v[132:133], v[132:133], s[14:15], v[12:13] op_sel_hi:[1,0,1]
	v_pk_fma_f32 v[2:3], v[128:129], s[14:15], v[16:17] op_sel_hi:[1,0,1]
	v_pk_mul_f32 v[0:1], v[132:133], v[4:5] op_sel_hi:[1,0]
	global_store_dwordx2 v[6:7], v[28:29], off
	global_store_dwordx2 v[8:9], v[30:31], off
	global_store_dwordx2 v[10:11], v[176:177], off
	v_pk_mul_f32 v[2:3], v[2:3], v[4:5] op_sel_hi:[1,0]
	v_mov_b32_e32 v28, 0
	v_mov_b32_e32 v29, 0
	v_cvt_pk_fp8_f32 v28, v0, v1
	v_cvt_pk_fp8_f32 v29, v2, v3
	v_pk_fma_f32 v[134:135], v[134:135], s[14:15], v[14:15] op_sel_hi:[1,0,1]
	v_pk_fma_f32 v[0:1], v[130:131], s[14:15], v[18:19] op_sel_hi:[1,0,1]
	v_pk_mul_f32 v[134:135], v[134:135], v[4:5] op_sel_hi:[1,0]
	v_pk_mul_f32 v[0:1], v[0:1], v[4:5] op_sel_hi:[1,0]
	v_cvt_pk_fp8_f32 v28, v134, v135 op_sel:[0,0,1]
	v_cvt_pk_fp8_f32 v29, v0, v1 op_sel:[0,0,1]
	v_lshlrev_b64 v[0:1], 11, v[20:21]
	v_lshl_add_u64 v[0:1], s[2:3], 0, v[0:1]
	v_lshl_add_u64 v[20:21], v[0:1], 0, v[24:25]
	v_mul_f32_e32 v30, 0x41800000, v179
	v_pk_fma_f32 v[120:121], v[120:121], s[14:15], v[16:17] op_sel_hi:[1,0,1]
	global_store_dwordx2 v[20:21], v[28:29], off
	v_pk_fma_f32 v[28:29], v[124:125], s[14:15], v[12:13] op_sel_hi:[1,0,1]
	v_pk_mul_f32 v[120:121], v[120:121], v[30:31] op_sel_hi:[1,0]
	v_mov_b32_e32 v125, 0
	v_cvt_pk_fp8_f32 v125, v120, v121
	v_pk_mul_f32 v[28:29], v[28:29], v[30:31] op_sel_hi:[1,0]
	v_mov_b32_e32 v124, 0
	v_cvt_pk_fp8_f32 v124, v28, v29
	v_pk_fma_f32 v[28:29], v[122:123], s[14:15], v[18:19] op_sel_hi:[1,0,1]
	ds_read2_b32 v[120:121], v181 offset0:144 offset1:160
	v_pk_mul_f32 v[28:29], v[28:29], v[30:31] op_sel_hi:[1,0]
	v_pk_fma_f32 v[2:3], v[126:127], s[14:15], v[14:15] op_sel_hi:[1,0,1]
	v_cvt_pk_fp8_f32 v125, v28, v29 op_sel:[0,0,1]
	ds_read2_b32 v[28:29], v23 offset0:144 offset1:160
	v_pk_mul_f32 v[2:3], v[2:3], v[30:31] op_sel_hi:[1,0]
	v_pk_fma_f32 v[112:113], v[112:113], s[14:15], v[16:17] op_sel_hi:[1,0,1]
	v_cvt_pk_fp8_f32 v124, v2, v3 op_sel:[0,0,1]
	v_pk_fma_f32 v[116:117], v[116:117], s[14:15], v[12:13] op_sel_hi:[1,0,1]
	s_waitcnt lgkmcnt(0)
; __device__ __forceinline__ unsigned pk4f8(float a, float b, float c, float d) { int r = 0; r = __builtin_amdgcn_cvt_pk_fp8_f32(a, b, r, false); r = __builtin_amdgcn_cvt_pk_fp8_f32(c, d, r, true); return (unsigned)r; }
;     __device__ __forceinline__ void operator()(const f32x4 (&acc)[2][2][4][2], const Unit& u, int wr, int wc, int fr, int fq) const {
;     ...
;         for (int bj = 0; bj < 2; ++bj) { const f32x4 b0 = *(const f32x4*)(bp + bj * HALF), b1 = *(const f32x4*)(bp + bj * HALF + 4);
; #pragma unroll
;             for (int ai = 0; ai < 2; ++ai)
; #pragma unroll
;                 for (int m = 0; m < 4; ++m) { const int r = u.ord * 256 + ai * HALF + wr * 64 + m * 16 + fr;
;                     const int dst = rowdst[r]; const float w = rowwt[r];
;                     const f32x4 v0 = (acc[ai][bj][m][0] * DS + b0) * (w * F8_SY), v1 = (acc[ai][bj][m][1] * DS + b1) * (w * F8_SY);
;                     v2u o; o.x = pk4f8(v0[0], v0[1], v0[2], v0[3]); o.y = pk4f8(v1[0], v1[1], v1[2], v1[3]);
;                     *(v2u*)(YS + (size_t)dst * D + col0 + bj * HALF) = o; } }
	v_ashrrev_i32_e32 v3, 31, v28
	v_mov_b32_e32 v2, v28
	v_mul_f32_e32 v28, 0x41800000, v120
	v_pk_mul_f32 v[112:113], v[112:113], v[28:29] op_sel_hi:[1,0]
	v_mov_b32_e32 v123, 0
	v_pk_mul_f32 v[116:117], v[116:117], v[28:29] op_sel_hi:[1,0]
	v_mov_b32_e32 v122, 0
	v_cvt_pk_fp8_f32 v123, v112, v113
	v_pk_fma_f32 v[112:113], v[114:115], s[14:15], v[18:19] op_sel_hi:[1,0,1]
	v_pk_fma_f32 v[108:109], v[108:109], s[14:15], v[12:13] op_sel_hi:[1,0,1]
	v_mul_f32_e32 v114, 0x41800000, v121
	v_pk_fma_f32 v[100:101], v[100:101], s[14:15], v[16:17] op_sel_hi:[1,0,1]
	v_pk_fma_f32 v[12:13], v[96:97], s[14:15], v[12:13] op_sel_hi:[1,0,1]
	v_mul_f32_e32 v96, 0x41800000, v183
	v_pk_fma_f32 v[16:17], v[84:85], s[14:15], v[16:17] op_sel_hi:[1,0,1]
	v_cvt_pk_fp8_f32 v122, v116, v117
	v_pk_mul_f32 v[108:109], v[108:109], v[114:115] op_sel_hi:[1,0]
	v_pk_mul_f32 v[100:101], v[100:101], v[114:115] op_sel_hi:[1,0]
	v_mov_b32_e32 v116, 0
	v_mov_b32_e32 v117, 0
	v_pk_mul_f32 v[12:13], v[12:13], v[96:97] op_sel_hi:[1,0]
	v_pk_mul_f32 v[16:17], v[16:17], v[96:97] op_sel_hi:[1,0]
	v_mov_b32_e32 v84, 0
	v_mov_b32_e32 v85, 0
	v_cvt_pk_fp8_f32 v116, v108, v109
	v_cvt_pk_fp8_f32 v117, v100, v101
	v_cvt_pk_fp8_f32 v84, v12, v13
	v_cvt_pk_fp8_f32 v85, v16, v17
	v_pk_fma_f32 v[118:119], v[118:119], s[14:15], v[14:15] op_sel_hi:[1,0,1]
	v_pk_fma_f32 v[110:111], v[110:111], s[14:15], v[14:15] op_sel_hi:[1,0,1]
	v_pk_fma_f32 v[100:101], v[102:103], s[14:15], v[18:19] op_sel_hi:[1,0,1]
	v_pk_fma_f32 v[14:15], v[98:99], s[14:15], v[14:15] op_sel_hi:[1,0,1]
	v_pk_fma_f32 v[12:13], v[86:87], s[14:15], v[18:19] op_sel_hi:[1,0,1]
	v_pk_mul_f32 v[118:119], v[118:119], v[28:29] op_sel_hi:[1,0]
	v_pk_mul_f32 v[112:113], v[112:113], v[28:29] op_sel_hi:[1,0]
	v_pk_mul_f32 v[110:111], v[110:111], v[114:115] op_sel_hi:[1,0]
	v_pk_mul_f32 v[100:101], v[100:101], v[114:115] op_sel_hi:[1,0]
	v_pk_mul_f32 v[14:15], v[14:15], v[96:97] op_sel_hi:[1,0]
	v_pk_mul_f32 v[12:13], v[12:13], v[96:97] op_sel_hi:[1,0]
	v_ashrrev_i32_e32 v1, 31, v5
	v_mov_b32_e32 v0, v5
	v_cvt_pk_fp8_f32 v122, v118, v119 op_sel:[0,0,1]
	v_cvt_pk_fp8_f32 v123, v112, v113 op_sel:[0,0,1]
	v_ashrrev_i32_e32 v113, 31, v29
	v_mov_b32_e32 v112, v29
	v_cvt_pk_fp8_f32 v116, v110, v111 op_sel:[0,0,1]
	v_cvt_pk_fp8_f32 v117, v100, v101 op_sel:[0,0,1]
	v_ashrrev_i32_e32 v23, 31, v22
	v_cvt_pk_fp8_f32 v84, v14, v15 op_sel:[0,0,1]
	v_cvt_pk_fp8_f32 v85, v12, v13 op_sel:[0,0,1]
	v_lshlrev_b64 v[0:1], 11, v[0:1]
	v_lshlrev_b64 v[2:3], 11, v[2:3]
	v_lshlrev_b64 v[100:101], 11, v[112:113]
	v_lshlrev_b64 v[12:13], 11, v[22:23]
	v_lshl_add_u64 v[0:1], s[2:3], 0, v[0:1]
	v_lshl_add_u64 v[2:3], s[2:3], 0, v[2:3]
	v_lshl_add_u64 v[100:101], s[2:3], 0, v[100:101]
	v_lshl_add_u64 v[12:13], s[2:3], 0, v[12:13]
	v_lshl_add_u64 v[0:1], v[0:1], 0, v[24:25]
	v_lshl_add_u64 v[2:3], v[2:3], 0, v[24:25]
	v_lshl_add_u64 v[100:101], v[100:101], 0, v[24:25]
	v_lshl_add_u64 v[22:23], v[12:13], 0, v[24:25]
	global_store_dwordx2 v[0:1], v[124:125], off
	global_store_dwordx2 v[2:3], v[122:123], off
	global_store_dwordx2 v[100:101], v[116:117], off
	global_store_dwordx2 v[22:23], v[84:85], off
	v_mov_b32_e32 v87, 0
	v_mov_b32_e32 v86, 0
	v_pk_fma_f32 v[26:27], v[104:105], s[14:15], v[238:239] op_sel_hi:[1,0,1]
	v_pk_fma_f32 v[84:85], v[92:93], s[14:15], v[242:243] op_sel_hi:[1,0,1]
	v_pk_mul_f32 v[26:27], v[178:179], v[26:27] op_sel_hi:[0,1]
	v_pk_mul_f32 v[84:85], v[178:179], v[84:85] op_sel_hi:[0,1]
	v_cvt_pk_fp8_f32 v87, v84, v85
	v_cvt_pk_fp8_f32 v86, v26, v27
	v_pk_fma_f32 v[26:27], v[94:95], s[14:15], v[244:245] op_sel_hi:[1,0,1]
	v_pk_fma_f32 v[80:81], v[80:81], s[14:15], v[242:243] op_sel_hi:[1,0,1]
	v_pk_mul_f32 v[26:27], v[178:179], v[26:27] op_sel_hi:[0,1]
	v_pk_mul_f32 v[80:81], v[180:181], v[80:81] op_sel_hi:[0,1]
	v_mov_b32_e32 v85, 0
	v_cvt_pk_fp8_f32 v87, v26, v27 op_sel:[0,0,1]
	v_pk_fma_f32 v[26:27], v[88:89], s[14:15], v[238:239] op_sel_hi:[1,0,1]
	v_cvt_pk_fp8_f32 v85, v80, v81
	v_pk_mul_f32 v[26:27], v[180:181], v[26:27] op_sel_hi:[0,1]
	v_mov_b32_e32 v84, 0
	v_cvt_pk_fp8_f32 v84, v26, v27
	v_pk_fma_f32 v[26:27], v[82:83], s[14:15], v[244:245] op_sel_hi:[1,0,1]
	v_pk_fma_f32 v[72:73], v[72:73], s[14:15], v[242:243] op_sel_hi:[1,0,1]
	v_pk_mul_f32 v[26:27], v[180:181], v[26:27] op_sel_hi:[0,1]
	v_cvt_pk_fp8_f32 v85, v26, v27 op_sel:[0,0,1]
	v_pk_fma_f32 v[26:27], v[76:77], s[14:15], v[238:239] op_sel_hi:[1,0,1]
	v_pk_mul_f32 v[72:73], v[182:183], v[72:73] op_sel_hi:[0,1]
	v_mov_b32_e32 v77, 0
	v_cvt_pk_fp8_f32 v77, v72, v73
	v_pk_mul_f32 v[26:27], v[182:183], v[26:27] op_sel_hi:[0,1]
	v_mov_b32_e32 v76, 0
	v_pk_fma_f32 v[24:25], v[106:107], s[14:15], v[240:241] op_sel_hi:[1,0,1]
	v_cvt_pk_fp8_f32 v76, v26, v27
; #define PG8_BAR __builtin_amdgcn_s_barrier()
; __device__ __forceinline__ unsigned pk4f8(float a, float b, float c, float d) { int r = 0; r = __builtin_amdgcn_cvt_pk_fp8_f32(a, b, r, false); r = __builtin_amdgcn_cvt_pk_fp8_f32(c, d, r, true); return (unsigned)r; }
; template <class Epi, class Sched, bool ALIGN_EPI = false, bool SP2 = false, bool FP8 = false, bool I8 = false>
; __device__ __forceinline__ void gemm_phase(PG8_LAS unsigned char* lds, const Gemm g, const Sched& S, const Epi& E) {
;     ...
;         if (!has_next) break;
; #pragma unroll
;         for (int a = 0; a < 2; ++a)
; #pragma unroll
;             for (int b = 0; b < 2; ++b)
; #pragma unroll
;                 for (int m = 0; m < 4; ++m)
; #pragma unroll
;                     for (int n = 0; n < 2; ++n) acc[a][b][m][n] = (f32x4){0.f, 0.f, 0.f, 0.f};
;         cur = nxt; cA = nA; cB = nB; ++ui;
;         if constexpr (ALIGN_EPI) { if (wr == 1) PG8_BAR; }
;     __device__ __forceinline__ void operator()(const f32x4 (&acc)[2][2][4][2], const Unit& u, int wr, int wc, int fr, int fq) const {
;     ...
;         for (int bj = 0; bj < 2; ++bj) { const f32x4 b0 = *(const f32x4*)(bp + bj * HALF), b1 = *(const f32x4*)(bp + bj * HALF + 4);
; #pragma unroll
;             for (int ai = 0; ai < 2; ++ai)
; #pragma unroll
;                 for (int m = 0; m < 4; ++m) { const int r = u.ord * 256 + ai * HALF + wr * 64 + m * 16 + fr;
;                     const int dst = rowdst[r]; const float w = rowwt[r];
;                     const f32x4 v0 = (acc[ai][bj][m][0] * DS + b0) * (w * F8_SY), v1 = (acc[ai][bj][m][1] * DS + b1) * (w * F8_SY);
;                     v2u o; o.x = pk4f8(v0[0], v0[1], v0[2], v0[3]); o.y = pk4f8(v1[0], v1[1], v1[2], v1[3]);
;                     *(v2u*)(YS + (size_t)dst * D + col0 + bj * HALF) = o; } }
	v_pk_fma_f32 v[26:27], v[74:75], s[14:15], v[244:245] op_sel_hi:[1,0,1]
	v_pk_mul_f32 v[24:25], v[178:179], v[24:25] op_sel_hi:[0,1]
	v_pk_mul_f32 v[26:27], v[182:183], v[26:27] op_sel_hi:[0,1]
	v_cvt_pk_fp8_f32 v86, v24, v25 op_sel:[0,0,1]
	v_pk_fma_f32 v[24:25], v[90:91], s[14:15], v[240:241] op_sel_hi:[1,0,1]
	v_cvt_pk_fp8_f32 v77, v26, v27 op_sel:[0,0,1]
	v_pk_fma_f32 v[26:27], v[68:69], s[14:15], v[238:239] op_sel_hi:[1,0,1]
	v_pk_fma_f32 v[64:65], v[64:65], s[14:15], v[242:243] op_sel_hi:[1,0,1]
	v_pk_mul_f32 v[24:25], v[180:181], v[24:25] op_sel_hi:[0,1]
	v_pk_mul_f32 v[26:27], v[4:5], v[26:27] op_sel_hi:[0,1]
	v_pk_mul_f32 v[64:65], v[4:5], v[64:65] op_sel_hi:[0,1]
	v_mov_b32_e32 v68, 0
	v_mov_b32_e32 v69, 0
	v_cvt_pk_fp8_f32 v84, v24, v25 op_sel:[0,0,1]
	v_pk_fma_f32 v[24:25], v[78:79], s[14:15], v[240:241] op_sel_hi:[1,0,1]
	v_cvt_pk_fp8_f32 v68, v26, v27
	v_cvt_pk_fp8_f32 v69, v64, v65
	v_pk_mul_f32 v[24:25], v[182:183], v[24:25] op_sel_hi:[0,1]
	v_cvt_pk_fp8_f32 v76, v24, v25 op_sel:[0,0,1]
	v_pk_fma_f32 v[24:25], v[70:71], s[14:15], v[240:241] op_sel_hi:[1,0,1]
	v_pk_fma_f32 v[26:27], v[66:67], s[14:15], v[244:245] op_sel_hi:[1,0,1]
	v_pk_mul_f32 v[24:25], v[4:5], v[24:25] op_sel_hi:[0,1]
	v_pk_mul_f32 v[4:5], v[4:5], v[26:27] op_sel_hi:[0,1]
	v_cvt_pk_fp8_f32 v68, v24, v25 op_sel:[0,0,1]
	v_cvt_pk_fp8_f32 v69, v4, v5 op_sel:[0,0,1]
	global_store_dwordx2 v[6:7], v[86:87], off offset:128
	global_store_dwordx2 v[8:9], v[84:85], off offset:128
	global_store_dwordx2 v[10:11], v[76:77], off offset:128
	global_store_dwordx2 v[20:21], v[68:69], off offset:128
	v_pk_fma_f32 v[8:9], v[56:57], s[14:15], v[242:243] op_sel_hi:[1,0,1]
	v_mov_b32_e32 v11, 0
	v_pk_mul_f32 v[8:9], v[30:31], v[8:9] op_sel_hi:[0,1]
	v_pk_fma_f32 v[6:7], v[60:61], s[14:15], v[238:239] op_sel_hi:[1,0,1]
	v_cvt_pk_fp8_f32 v11, v8, v9
	v_pk_mul_f32 v[6:7], v[30:31], v[6:7] op_sel_hi:[0,1]
	v_mov_b32_e32 v10, 0
	v_cvt_pk_fp8_f32 v10, v6, v7
	v_pk_fma_f32 v[6:7], v[58:59], s[14:15], v[244:245] op_sel_hi:[1,0,1]
	v_pk_fma_f32 v[8:9], v[48:49], s[14:15], v[242:243] op_sel_hi:[1,0,1]
	v_pk_mul_f32 v[6:7], v[30:31], v[6:7] op_sel_hi:[0,1]
	v_pk_mul_f32 v[8:9], v[28:29], v[8:9] op_sel_hi:[0,1]
	v_mov_b32_e32 v21, 0
	v_cvt_pk_fp8_f32 v11, v6, v7 op_sel:[0,0,1]
	v_pk_fma_f32 v[6:7], v[52:53], s[14:15], v[238:239] op_sel_hi:[1,0,1]
	v_cvt_pk_fp8_f32 v21, v8, v9
	v_pk_mul_f32 v[6:7], v[28:29], v[6:7] op_sel_hi:[0,1]
	v_mov_b32_e32 v20, 0
	v_cvt_pk_fp8_f32 v20, v6, v7
	v_pk_fma_f32 v[6:7], v[50:51], s[14:15], v[244:245] op_sel_hi:[1,0,1]
	v_pk_fma_f32 v[8:9], v[40:41], s[14:15], v[242:243] op_sel_hi:[1,0,1]
	v_pk_mul_f32 v[6:7], v[28:29], v[6:7] op_sel_hi:[0,1]
	v_pk_mul_f32 v[8:9], v[114:115], v[8:9] op_sel_hi:[0,1]
	v_mov_b32_e32 v25, 0
	v_cvt_pk_fp8_f32 v21, v6, v7 op_sel:[0,0,1]
	v_pk_fma_f32 v[6:7], v[44:45], s[14:15], v[238:239] op_sel_hi:[1,0,1]
	v_cvt_pk_fp8_f32 v25, v8, v9
	v_pk_mul_f32 v[6:7], v[114:115], v[6:7] op_sel_hi:[0,1]
	v_mov_b32_e32 v24, 0
	v_pk_fma_f32 v[4:5], v[62:63], s[14:15], v[240:241] op_sel_hi:[1,0,1]
	v_cvt_pk_fp8_f32 v24, v6, v7
	v_pk_fma_f32 v[6:7], v[42:43], s[14:15], v[244:245] op_sel_hi:[1,0,1]
	v_pk_mul_f32 v[4:5], v[30:31], v[4:5] op_sel_hi:[0,1]
	v_pk_mul_f32 v[6:7], v[114:115], v[6:7] op_sel_hi:[0,1]
	v_cvt_pk_fp8_f32 v10, v4, v5 op_sel:[0,0,1]
	v_pk_fma_f32 v[4:5], v[54:55], s[14:15], v[240:241] op_sel_hi:[1,0,1]
	v_cvt_pk_fp8_f32 v25, v6, v7 op_sel:[0,0,1]
	v_pk_fma_f32 v[6:7], v[36:37], s[14:15], v[238:239] op_sel_hi:[1,0,1]
	v_pk_fma_f32 v[8:9], v[32:33], s[14:15], v[242:243] op_sel_hi:[1,0,1]
	v_pk_mul_f32 v[4:5], v[28:29], v[4:5] op_sel_hi:[0,1]
	v_pk_mul_f32 v[6:7], v[96:97], v[6:7] op_sel_hi:[0,1]
	v_pk_mul_f32 v[8:9], v[96:97], v[8:9] op_sel_hi:[0,1]
	v_mov_b32_e32 v12, 0
	v_mov_b32_e32 v13, 0
	v_cvt_pk_fp8_f32 v20, v4, v5 op_sel:[0,0,1]
	v_pk_fma_f32 v[4:5], v[46:47], s[14:15], v[240:241] op_sel_hi:[1,0,1]
	v_cvt_pk_fp8_f32 v12, v6, v7
	v_cvt_pk_fp8_f32 v13, v8, v9
	v_pk_mul_f32 v[4:5], v[114:115], v[4:5] op_sel_hi:[0,1]
	v_cvt_pk_fp8_f32 v24, v4, v5 op_sel:[0,0,1]
	v_pk_fma_f32 v[4:5], v[38:39], s[14:15], v[240:241] op_sel_hi:[1,0,1]
	v_pk_fma_f32 v[6:7], v[34:35], s[14:15], v[244:245] op_sel_hi:[1,0,1]
	v_pk_mul_f32 v[4:5], v[96:97], v[4:5] op_sel_hi:[0,1]
	v_pk_mul_f32 v[6:7], v[96:97], v[6:7] op_sel_hi:[0,1]
	v_cvt_pk_fp8_f32 v12, v4, v5 op_sel:[0,0,1]
	v_cvt_pk_fp8_f32 v13, v6, v7 op_sel:[0,0,1]
	global_store_dwordx2 v[0:1], v[10:11], off offset:128
	global_store_dwordx2 v[2:3], v[20:21], off offset:128
	global_store_dwordx2 v[100:101], v[24:25], off offset:128
	global_store_dwordx2 v[22:23], v[12:13], off offset:128
	s_cbranch_vccnz .LBB0_2391
	s_andn2_b64 vcc, exec, s[0:1]
	s_cbranch_vccnz .LBB0_2390
	s_barrier
	s_branch .LBB0_2390
